# each kernel also touches the 4 KiB page around its kernarg block so the next launches' kernargs are L2-warm
# speedup vs baseline: 1.0365x; 1.0365x over previous
.LBB0_6:
	s_or_b64 exec, exec, s[4:5]
	s_waitcnt lgkmcnt(0)
	s_barrier
	ds_read_b32 v19, v29
	v_lshl_add_u32 v26, v26, s8, v27
	ds_read_b32 v27, v30
	ds_read_b32 v28, v28
	ds_read_b32 v25, v25
	s_waitcnt vmcnt(3)
	v_cmp_eq_u32_e32 vcc, 0, v17
	s_mov_b64 s[4:5], -1
	s_waitcnt lgkmcnt(3)
	v_add_lshl_u32 v19, v26, v19, 2
	ds_write2st64_b32 v19, v8, v9 offset1:64
	v_bfrev_b32_e32 v8, 1
	v_cndmask_b32_e32 v8, 0, v8, vcc
	v_or_b32_e32 v8, v8, v0
	ds_write_b32 v19, v8 offset:32768
	v_lshl_add_u32 v8, v20, s8, v21
	s_waitcnt lgkmcnt(4)
	v_add_lshl_u32 v8, v8, v27, 2
	ds_write2st64_b32 v8, v4, v5 offset1:64
	v_mov_b32_e32 v4, 0x400
	v_mov_b32_e32 v5, 0x80000400
	s_waitcnt vmcnt(2)
	v_cmp_eq_u32_e32 vcc, 0, v16
	s_nop 1
	v_cndmask_b32_e32 v4, v4, v5, vcc
	v_or_b32_e32 v4, v4, v0
	ds_write_b32 v8, v4 offset:32768
	v_lshl_add_u32 v4, v22, s8, v23
	s_waitcnt lgkmcnt(5)
	v_add_lshl_u32 v4, v4, v28, 2
	ds_write2st64_b32 v4, v6, v7 offset1:64
	v_mov_b32_e32 v5, 0x800
	v_mov_b32_e32 v6, 0x80000800
	s_waitcnt vmcnt(1)
	v_cmp_eq_u32_e32 vcc, 0, v15
	s_nop 1
	v_cndmask_b32_e32 v5, v5, v6, vcc
	v_or_b32_e32 v5, v5, v0
	ds_write_b32 v4, v5 offset:32768
	v_lshl_add_u32 v4, v24, s8, v18
	s_waitcnt lgkmcnt(6)
	v_add_lshl_u32 v4, v4, v25, 2
	ds_write2st64_b32 v4, v2, v3 offset1:64
	v_mov_b32_e32 v2, 0xc00
	v_mov_b32_e32 v3, 0x80000c00
	s_waitcnt vmcnt(0)
	v_cmp_eq_u32_e32 vcc, 0, v14
	s_nop 1
	v_cndmask_b32_e32 v2, v2, v3, vcc
	v_or_b32_e32 v2, v2, v0
	ds_write_b32 v4, v2 offset:32768
	s_waitcnt lgkmcnt(0)
	s_barrier
	s_getpc_b64 s[30:31]
	s_add_u32 s30, s30, 0x24b8
	s_addc_u32 s31, s31, 0
	v_lshlrev_b32_e32 v40, 6, v0
	v_min_u32_e32 v40, 0x2d00, v40
	global_load_dword v40, v40, s[30:31]
	s_and_b32 s32, s0, 0xfffff000
	s_mov_b32 s33, s1
	v_and_b32_e32 v41, 63, v0
	v_lshlrev_b32_e32 v41, 6, v41
	global_load_dword v41, v41, s[32:33]
	ds_read_b32 v14, v11 offset:32768
	s_mov_b64 s[18:19], s[44:45]
	s_mov_b64 s[8:9], s[36:37]
	s_mov_b64 s[10:11], s[38:39]
	s_mov_b64 s[12:13], s[40:41]
	s_mov_b64 s[14:15], s[42:43]
	ds_read2st64_b32 v[4:5], v11 offset1:64
	v_or_b32_e32 v2, s16, v0
	v_mov_b32_e32 v3, 0
	s_waitcnt lgkmcnt(0)
	v_and_b32_e32 v15, 0x7fffffff, v14
	s_and_b64 vcc, exec, s[2:3]
	v_lshlrev_b64 v[6:7], 2, v[2:3]
	s_cbranch_vccz .LBB0_8
	v_lshl_add_u64 v[8:9], s[10:11], 0, v[6:7]
	global_store_dword v[8:9], v4, off
	v_lshl_add_u64 v[8:9], s[12:13], 0, v[6:7]
	global_store_dword v[8:9], v5, off
	v_lshl_add_u64 v[8:9], s[14:15], 0, v[6:7]
	global_store_dword v[8:9], v15, off
	s_mov_b64 s[4:5], 0

_Z6k_iterILb1ELb0EEvPKfS1_PKiPK15HIP_vector_typeIfLj4EES7_S1_S1_S3_S1_PfS8_S1_S3_PDF16_PS5_SA_PiSA_SB_:
	s_and_b32 s96, s0, 0xfffff000
	s_mov_b32 s97, s1
	s_load_dwordx2 s[4:5], s[0:1], 0x78
	s_load_dwordx8 s[20:27], s[0:1], 0x20
	s_load_dwordx2 s[92:93], s[0:1], 0x18
	s_load_dwordx2 s[48:49], s[0:1], 0x90
	s_load_dwordx2 s[50:51], s[0:1], 0x80
	s_load_dwordx4 s[28:31], s[0:1], 0x60
	v_readfirstlane_b32 s54, v0
	v_cmp_gt_u32_e64 s[8:9], 64, v0
	v_lshlrev_b32_e32 v46, 2, v0
	s_and_saveexec_b64 s[6:7], s[8:9]
	v_mov_b32_e32 v1, 0
	ds_write_b32 v46, v1 offset:29728
	s_or_b64 exec, exec, s[6:7]
	s_lshl_b32 s3, s2, 5
	s_and_b32 s3, s3, 0xe0
	s_lshr_b32 s2, s2, 3
	s_add_i32 s46, s3, s2
	s_lshr_b32 s12, s46, 6
	s_lshl_b32 s13, s46, 6
	s_mov_b32 s47, 0
	s_and_b32 s33, s13, 0xfc0
	s_lshl_b32 s58, s12, 12
	s_lshl_b64 s[2:3], s[46:47], 4
	s_waitcnt lgkmcnt(0)
	s_add_u32 s6, s20, s2
	v_and_b32_e32 v25, 31, v0
	s_addc_u32 s7, s21, s3
	s_or_b32 s59, s58, s33
	v_or_b32_e32 v6, s59, v25
	v_mov_b32_e32 v7, 0
	v_lshlrev_b64 v[2:3], 2, v[6:7]
	v_lshl_add_u64 v[4:5], s[22:23], 0, v[2:3]
	v_lshl_add_u64 v[8:9], s[24:25], 0, v[2:3]
	v_lshl_add_u64 v[2:3], s[26:27], 0, v[2:3]
	global_load_dword v196, v[4:5], off offset:128
	global_load_dword v197, v[8:9], off offset:128
	global_load_dword v198, v[2:3], off offset:128
	global_load_dword v4, v[4:5], off
	global_load_dword v5, v[8:9], off
	global_load_dword v6, v[2:3], off
	s_lshl_b32 s94, s12, 13
	s_add_u32 s94, s92, s94
	s_addc_u32 s95, s93, 0
	v_lshlrev_b32_e32 v199, 4, v0
	global_load_dwordx4 v[192:195], v199, s[94:95]
	s_load_dwordx4 s[36:39], s[6:7], 0x0
	s_load_dwordx2 s[34:35], s[0:1], 0x48
	s_load_dwordx4 s[40:43], s[0:1], 0x0
	s_load_dwordx2 s[52:53], s[0:1], 0x10
	s_load_dwordx2 s[98:99], s[0:1], 0x88
	s_load_dwordx2 s[100:101], s[0:1], 0x58
	s_bfe_u32 s14, s54, 0x10006
	s_cmpk_lt_u32 s54, 0x80
	s_cselect_b64 s[6:7], -1, 0
	s_waitcnt lgkmcnt(0)
	v_mov_b64_e32 v[2:3], s[38:39]
	v_pk_add_f32 v[2:3], s[36:37], v[2:3]
	s_cmp_eq_u32 s14, 0
	v_pk_mul_f32 v[22:23], v[2:3], 0.5 op_sel_hi:[1,0]
	v_and_b32_e32 v44, 63, v0
	s_cselect_b64 s[10:11], -1, 0
	v_mov_b32_e32 v1, 0xff800000
	v_cmp_gt_u32_e64 s[18:19], 32, v44
	s_and_b64 s[10:11], s[10:11], s[6:7]
	s_and_b64 s[16:17], s[10:11], s[18:19]
	v_lshlrev_b32_e32 v10, 4, v25
	s_waitcnt vmcnt(2)
	v_pk_fma_f32 v[36:37], v[2:3], 0.5, v[4:5] op_sel_hi:[1,0,1] neg_lo:[1,0,0] neg_hi:[1,0,0]
	s_nop 0
	v_pk_mul_f32 v[2:3], v[36:37], v[36:37]
	s_waitcnt vmcnt(1)
	v_cmp_ne_u32_e32 vcc, 0, v6
	v_add_f32_e32 v2, v2, v3
	v_sub_f32_e32 v2, 0x3d23d70a, v2
	v_mul_f32_e32 v2, 0x431044f5, v2
	v_cndmask_b32_e32 v4, v1, v2, vcc
	s_and_saveexec_b64 s[10:11], s[16:17]
	s_cbranch_execz .LBB2_4
	s_mov_b32 s16, 0x439044f5
	v_or_b32_e32 v6, s13, v25
	v_pk_mul_f32 v[2:3], v[36:37], s[16:17] op_sel_hi:[1,0]
	v_mov_b32_e32 v5, v7
	v_lshl_add_u64 v[8:9], v[6:7], 4, s[4:5]
	ds_write_b128 v10, v[2:5] offset:26656
	global_store_dwordx4 v[8:9], v[2:5], off sc1

.Lfirst_pc:
	s_add_u32 s66, s66, (.Lfirst_code_end-.Lfirst_pc)&4294967295
	s_addc_u32 s67, s67, 0
	s_lshl_b32 s68, s27, 12
	v_lshl_or_b32 v214, v44, 6, s68
	v_min_u32_e32 v214, 0x3300, v214
	global_load_dword v214, v214, s[66:67]
	v_lshlrev_b32_e32 v215, 6, v44
	global_load_dword v215, v215, s[96:97]
	s_andn2_b64 vcc, exec, s[0:1]
	s_waitcnt lgkmcnt(0)
	s_barrier
	s_cbranch_vccnz .LBB2_117
	v_lshlrev_b32_e32 v0, 3, v1
	v_add_u32_e32 v0, 0x7000, v0
	ds_read2_b64 v[12:15], v0 offset0:196 offset1:198
	ds_read2_b64 v[8:11], v0 offset0:200 offset1:202
	ds_read2_b64 v[4:7], v0 offset0:204 offset1:206
	ds_read2_b64 v[0:3], v0 offset0:208 offset1:210
	v_mov_b32_e32 v21, 0
	ds_read_b32 v36, v21 offset:30368
	s_cmp_lt_i32 s39, 4
	s_mov_b64 s[0:1], 0
	s_cbranch_scc1 .LBB2_118
	s_cmp_gt_i32 s39, 4
	s_cbranch_scc0 .LBB2_119
	s_cmp_gt_i32 s39, 5
	s_cbranch_scc0 .LBB2_129
	s_mov_b64 s[8:9], 0
	s_cmp_eq_u32 s39, 6
	s_mov_b64 s[14:15], 0
	s_cbranch_scc0 .LBB2_107
	v_mov_b32_e32 v37, 0
	s_waitcnt lgkmcnt(4)
	v_dot2c_f32_f16_e32 v37, v20, v12
	v_mov_b32_e32 v20, 0
	v_dot2c_f32_f16_e32 v20, v49, v13
	v_dot2c_f32_f16_e32 v37, v54, v14
	v_dot2c_f32_f16_e32 v20, v57, v15
	s_waitcnt lgkmcnt(3)
	v_dot2c_f32_f16_e32 v37, v61, v8
	v_dot2c_f32_f16_e32 v20, v64, v9
	v_dot2c_f32_f16_e32 v37, v67, v10
	v_dot2c_f32_f16_e32 v20, v69, v11
	s_waitcnt lgkmcnt(2)
	v_dot2c_f32_f16_e32 v37, v75, v4
	v_dot2c_f32_f16_e32 v20, v79, v5
	v_dot2c_f32_f16_e32 v37, v85, v6
	v_dot2c_f32_f16_e32 v20, v88, v7
	s_waitcnt lgkmcnt(1)
	v_dot2c_f32_f16_e32 v37, v91, v0
	v_dot2c_f32_f16_e32 v20, v94, v1
	v_dot2c_f32_f16_e32 v37, v97, v2
	v_dot2c_f32_f16_e32 v20, v98, v3
	s_and_b64 vcc, s[18:19], s[12:13]
	v_cndmask_b32_e32 v35, -1, v35, vcc
	v_mov_b32_e32 v21, 0
	v_add_f32_e32 v20, v37, v20
	v_mov_b32_e32 v37, v20
	s_nop 1
	v_permlane32_swap_b32_e32 v20, v37
	v_cmp_lt_i32_e32 vcc, -1, v35
	s_and_saveexec_b64 s[12:13], vcc
	s_cbranch_execz .LBB2_106
	v_add_f32_e32 v20, v20, v37
	s_waitcnt lgkmcnt(0)
	v_mul_f32_e32 v37, v36, v20
	v_add_u32_e32 v20, s58, v35
	v_lshl_add_u64 v[20:21], v[20:21], 2, s[34:35]
	global_atomic_add_f32 v[20:21], v37, off

_Z6k_iterILb0ELb0EEvPKfS1_PKiPK15HIP_vector_typeIfLj4EES7_S1_S1_S3_S1_PfS8_S1_S3_PDF16_PS5_SA_PiSA_SB_:
	s_and_b32 s38, s0, 0xfffff000
	s_mov_b32 s39, s1
	s_load_dwordx2 s[8:9], s[0:1], 0x80
	s_load_dwordx4 s[4:7], s[0:1], 0x70
	s_load_dwordx4 s[16:19], s[0:1], 0x40
	v_readfirstlane_b32 s12, v0
	v_cmp_gt_u32_e64 s[14:15], 64, v0
	v_lshlrev_b32_e32 v1, 2, v0
	s_and_saveexec_b64 s[10:11], s[14:15]
	v_mov_b32_e32 v2, 0
	ds_write_b32 v1, v2 offset:5152
	s_or_b64 exec, exec, s[10:11]
	s_lshl_b32 s3, s2, 5
	s_and_b32 s3, s3, 0xe0
	s_lshr_b32 s2, s2, 3
	s_add_i32 s2, s3, s2
	s_lshl_b32 s25, s2, 6
	v_and_b32_e32 v2, 31, v0
	v_or_b32_e32 v4, s25, v2
	v_mov_b32_e32 v5, 0
	s_lshr_b32 s27, s12, 6
	s_lshl_b32 s32, s27, 2
	s_lshr_b32 s32, 0x73261540, s32
	s_lshl_b32 s32, s32, 5
	s_and_b32 s32, s32, 0xe0
	v_or_b32_e32 v176, s32, v2
	v_lshlrev_b32_e32 v177, 4, v176
	v_add_u32_e32 v178, 0x1000, v177
	v_add_u32_e32 v179, 0x2000, v177
	v_add_u32_e32 v180, 0x3000, v177
	v_add_u32_e32 v181, 0x4000, v177
	v_add_u32_e32 v182, 0x5000, v177
	s_mov_b32 s3, 0
	s_lshl_b64 s[34:35], s[2:3], 16
	s_lshl_b32 s33, s2, 2
	s_waitcnt lgkmcnt(0)
	s_load_dword s24, s[8:9], s33 offset:0x0
	s_add_u32 s20, s4, s34
	s_addc_u32 s21, s5, s35
	v_lshl_add_u64 v[4:5], v[4:5], 4, s[6:7]
	global_load_dwordx3 v[30:32], v[4:5], off
	global_load_dwordx3 v[26:28], v[4:5], off offset:512
	global_load_dwordx4 v[2:5], v177, s[20:21]
	global_load_dwordx4 v[6:9], v178, s[20:21]
	global_load_dwordx4 v[10:13], v179, s[20:21]
	global_load_dwordx4 v[14:17], v180, s[20:21]
	global_load_dwordx4 v[18:21], v181, s[20:21]
	global_load_dwordx4 v[22:25], v182, s[20:21]
	v_and_b32_e32 v38, 63, v0
	v_mov_b32_e32 v29, 0xff800000
	v_cmp_gt_u32_e64 s[0:1], 32, v38
	s_waitcnt lgkmcnt(0)
	s_cmpk_gt_i32 s24, 0x600
	s_cselect_b64 s[22:23], -1, 0
	s_cmpk_lt_i32 s24, 0x601
	s_cbranch_scc1 .LBB3_6
	s_and_saveexec_b64 s[8:9], s[14:15]
	s_cbranch_execz .LBB3_5
	v_or_b32_e32 v178, s25, v0
	v_mov_b32_e32 v179, 0
	v_lshl_add_u64 v[178:179], v[178:179], 4, s[6:7]
	global_load_dwordx4 v[178:181], v[178:179], off
	v_lshlrev_b32_e32 v177, 4, v0
	s_waitcnt vmcnt(0)
	ds_write_b128 v177, v[178:181] offset:2080

.Lff_pc:
	s_add_u32 s36, s36, (.Lff_code_end-.Lff_pc)&4294967295
	s_addc_u32 s37, s37, 0
	v_lshlrev_b32_e32 v183, 6, v0
	v_min_u32_e32 v183, 0x3300, v183
	global_load_dword v183, v183, s[36:37]
	v_lshlrev_b32_e32 v182, 6, v38
	global_load_dword v182, v182, s[38:39]
	s_mov_b32 s4, 0x42c80000
	v_cndmask_b32_e32 v3, 0, v3, vcc
	v_cmp_lt_f32_e32 vcc, 0, v131
	v_cmp_ngt_f32_e64 s[2:3], s4, v3
	s_mov_b64 s[6:7], 0
	v_cndmask_b32_e32 v4, 0, v4, vcc
	v_cmp_lt_f32_e32 vcc, 0, v130
	s_nop 1
	v_cndmask_b32_e32 v5, 0, v5, vcc
	v_cmp_lt_f32_e32 vcc, 0, v129
	s_nop 1
	v_cndmask_b32_e32 v6, 0, v6, vcc
	v_cmp_lt_f32_e32 vcc, 0, v128
	s_nop 1
	v_cndmask_b32_e32 v7, 0, v7, vcc
	v_cmp_ngt_f32_e32 vcc, s4, v2
	s_or_b64 s[2:3], vcc, s[2:3]
	v_cmp_ngt_f32_e32 vcc, s4, v4
	s_or_b64 s[2:3], s[2:3], vcc
	v_cmp_ngt_f32_e32 vcc, s4, v5
	s_or_b64 s[2:3], s[2:3], vcc
	v_cmp_ngt_f32_e32 vcc, s4, v6
	s_or_b64 s[2:3], s[2:3], vcc
	v_cmp_ngt_f32_e32 vcc, s4, v7
	s_or_b64 s[2:3], s[2:3], vcc
	v_cndmask_b32_e64 v8, 0, 1, s[2:3]
	v_cmp_ne_u32_e32 vcc, 0, v8
	s_cmp_eq_u64 vcc, 0
	s_cselect_b64 s[2:3], -1, 0
	v_cndmask_b32_e64 v8, 0, 1, s[2:3]
	s_nop 0
	v_readfirstlane_b32 s2, v8
	s_bitcmp0_b32 s2, 0
	s_cbranch_scc0 .LBB3_45
	s_cmp_lt_i32 s26, 4
	s_cbranch_scc1 .LBB3_46
	s_cmp_gt_i32 s26, 4
	s_cbranch_scc0 .LBB3_47
	s_mov_b64 s[4:5], -1
	v_mov_b32_e32 v8, 0
	s_cmp_gt_i32 s26, 5
	v_mov_b32_e32 v167, 0
	v_mov_b32_e32 v166, 0
	v_mov_b32_e32 v165, 0
	v_mov_b32_e32 v164, 0
	v_mov_b32_e32 v162, 0
	v_mov_b32_e32 v160, 0
	v_mov_b32_e32 v159, 0
	v_mov_b32_e32 v157, 0
	v_mov_b32_e32 v151, 0
	v_mov_b32_e32 v149, 0
	v_mov_b32_e32 v147, 0
	v_mov_b32_e32 v146, 0
	v_mov_b32_e32 v144, 0
	v_mov_b32_e32 v143, 0
	v_mov_b32_e32 v152, 0
	v_mov_b32_e32 v153, 0
	v_mov_b32_e32 v154, 0
	v_mov_b32_e32 v155, 0
	v_mov_b32_e32 v156, 0
	v_mov_b32_e32 v158, 0
	v_mov_b32_e32 v161, 0
	v_mov_b32_e32 v163, 0
	v_mov_b32_e32 v168, 0
	v_mov_b32_e32 v169, 0
	v_mov_b32_e32 v170, 0
	v_mov_b32_e32 v171, 0
	v_mov_b32_e32 v172, 0
	v_mov_b32_e32 v173, 0
	v_mov_b32_e32 v174, 0
	v_mov_b32_e32 v145, 0
	v_mov_b32_e32 v148, 0
	v_mov_b32_e32 v150, 0
	s_cbranch_scc0 .LBB3_50
	s_cmp_eq_u32 s26, 6
	s_cbranch_scc0 .LBB3_49
	v_mov_b32_e32 v145, 0
	v_mov_b32_e32 v148, 0
	v_mov_b32_e32 v150, 0
	v_mov_b32_e32 v143, 0
	v_mov_b32_e32 v144, 0
	v_mov_b32_e32 v146, 0
	v_mov_b32_e32 v147, 0
	v_mov_b32_e32 v149, 0
	v_mov_b32_e32 v151, 0
	v_mov_b32_e32 v152, 0
	v_mov_b32_e32 v153, 0
	v_mov_b32_e32 v154, 0
	v_mov_b32_e32 v155, 0
	v_mov_b32_e32 v156, 0
	v_mov_b32_e32 v158, 0
	v_mov_b32_e32 v161, 0
	v_mov_b32_e32 v163, 0
	v_mov_b32_e32 v157, 0
	v_mov_b32_e32 v159, 0
	v_mov_b32_e32 v160, 0
	v_mov_b32_e32 v162, 0
	v_mov_b32_e32 v164, 0
	v_mov_b32_e32 v165, 0
	v_mov_b32_e32 v166, 0
	v_mov_b32_e32 v167, 0
	v_mov_b32_e32 v168, 0
	v_mov_b32_e32 v169, 0
	v_mov_b32_e32 v170, 0
	v_mov_b32_e32 v171, 0
	v_mov_b32_e32 v172, 0
	v_mov_b32_e32 v173, 0
	v_mov_b32_e32 v174, 0
	v_fma_mix_f32 v148, v43, v7, v148 op_sel_hi:[1,0,0]
	v_fma_mix_f32 v150, v45, v7, v150 op_sel_hi:[1,0,0]
	v_fma_mix_f32 v143, v50, v7, v143 op_sel_hi:[1,0,0]
	v_fma_mix_f32 v144, v54, v7, v144 op_sel_hi:[1,0,0]
	v_fma_mix_f32 v146, v58, v7, v146 op_sel_hi:[1,0,0]
	v_fma_mix_f32 v147, v61, v7, v147 op_sel_hi:[1,0,0]
	v_fma_mix_f32 v149, v64, v7, v149 op_sel_hi:[1,0,0]
	v_fma_mix_f32 v151, v66, v7, v151 op_sel_hi:[1,0,0]
	v_fma_mix_f32 v152, v43, v7, v152 op_sel:[1,0,0] op_sel_hi:[1,0,0]
	v_fma_mix_f32 v153, v45, v7, v153 op_sel:[1,0,0] op_sel_hi:[1,0,0]
	v_fma_mix_f32 v154, v50, v7, v154 op_sel:[1,0,0] op_sel_hi:[1,0,0]
	v_fma_mix_f32 v155, v54, v7, v155 op_sel:[1,0,0] op_sel_hi:[1,0,0]
	v_fma_mix_f32 v156, v58, v7, v156 op_sel:[1,0,0] op_sel_hi:[1,0,0]
	v_fma_mix_f32 v158, v61, v7, v158 op_sel:[1,0,0] op_sel_hi:[1,0,0]
	v_fma_mix_f32 v161, v64, v7, v161 op_sel:[1,0,0] op_sel_hi:[1,0,0]
	v_fma_mix_f32 v163, v66, v7, v163 op_sel:[1,0,0] op_sel_hi:[1,0,0]
	v_fma_mix_f32 v157, v72, v7, v157 op_sel_hi:[1,0,0]
	v_fma_mix_f32 v159, v76, v7, v159 op_sel_hi:[1,0,0]
	v_fma_mix_f32 v160, v83, v7, v160 op_sel_hi:[1,0,0]
	v_fma_mix_f32 v162, v85, v7, v162 op_sel_hi:[1,0,0]
	v_fma_mix_f32 v164, v89, v7, v164 op_sel_hi:[1,0,0]
	v_fma_mix_f32 v165, v92, v7, v165 op_sel_hi:[1,0,0]
	v_fma_mix_f32 v166, v95, v7, v166 op_sel_hi:[1,0,0]
	v_fma_mix_f32 v167, v96, v7, v167 op_sel_hi:[1,0,0]
	v_fma_mix_f32 v168, v72, v7, v168 op_sel:[1,0,0] op_sel_hi:[1,0,0]
	v_fma_mix_f32 v169, v76, v7, v169 op_sel:[1,0,0] op_sel_hi:[1,0,0]
	v_fma_mix_f32 v170, v83, v7, v170 op_sel:[1,0,0] op_sel_hi:[1,0,0]
	v_fma_mix_f32 v171, v85, v7, v171 op_sel:[1,0,0] op_sel_hi:[1,0,0]
	v_fma_mix_f32 v172, v89, v7, v172 op_sel:[1,0,0] op_sel_hi:[1,0,0]
	v_fma_mix_f32 v173, v92, v7, v173 op_sel:[1,0,0] op_sel_hi:[1,0,0]
	v_fma_mix_f32 v174, v95, v7, v174 op_sel:[1,0,0] op_sel_hi:[1,0,0]
	v_fma_mix_f32 v145, v96, v7, v145 op_sel:[1,0,0] op_sel_hi:[1,0,0]
	s_branch .LBB3_50

_Z6k_iterILb0ELb1EEvPKfS1_PKiPK15HIP_vector_typeIfLj4EES7_S1_S1_S3_S1_PfS8_S1_S3_PDF16_PS5_SA_PiSA_SB_:
	s_and_b32 s38, s0, 0xfffff000
	s_mov_b32 s39, s1
	s_load_dwordx2 s[8:9], s[0:1], 0x80
	s_load_dwordx4 s[4:7], s[0:1], 0x70
	s_load_dwordx4 s[16:19], s[0:1], 0x40
	s_load_dwordx2 s[22:23], s[0:1], 0x50
	v_readfirstlane_b32 s12, v0
	v_cmp_gt_u32_e64 s[14:15], 64, v0
	v_lshlrev_b32_e32 v1, 2, v0
	s_and_saveexec_b64 s[10:11], s[14:15]
	v_mov_b32_e32 v2, 0
	ds_write_b32 v1, v2 offset:5152
	s_or_b64 exec, exec, s[10:11]
	s_lshl_b32 s3, s2, 5
	s_and_b32 s3, s3, 0xe0
	s_lshr_b32 s2, s2, 3
	s_add_i32 s2, s3, s2
	s_lshl_b32 s29, s2, 6
	v_and_b32_e32 v2, 31, v0
	v_or_b32_e32 v4, s29, v2
	v_mov_b32_e32 v5, 0
	s_lshr_b32 s30, s12, 6
	s_lshl_b32 s32, s30, 2
	s_lshr_b32 s32, 0x73261540, s32
	s_lshl_b32 s32, s32, 5
	s_and_b32 s32, s32, 0xe0
	v_or_b32_e32 v176, s32, v2
	v_lshlrev_b32_e32 v177, 4, v176
	v_add_u32_e32 v178, 0x1000, v177
	v_add_u32_e32 v179, 0x2000, v177
	v_add_u32_e32 v180, 0x3000, v177
	v_add_u32_e32 v181, 0x4000, v177
	v_add_u32_e32 v182, 0x5000, v177
	s_mov_b32 s3, 0
	s_lshl_b64 s[34:35], s[2:3], 16
	s_lshl_b32 s33, s2, 2
	s_waitcnt lgkmcnt(0)
	s_load_dword s26, s[8:9], s33 offset:0x0
	s_add_u32 s20, s4, s34
	s_addc_u32 s21, s5, s35
	v_lshl_add_u64 v[4:5], v[4:5], 4, s[6:7]
	global_load_dwordx3 v[30:32], v[4:5], off
	global_load_dwordx3 v[26:28], v[4:5], off offset:512
	global_load_dwordx4 v[2:5], v177, s[20:21]
	global_load_dwordx4 v[6:9], v178, s[20:21]
	global_load_dwordx4 v[10:13], v179, s[20:21]
	global_load_dwordx4 v[14:17], v180, s[20:21]
	global_load_dwordx4 v[18:21], v181, s[20:21]
	global_load_dwordx4 v[22:25], v182, s[20:21]
	v_and_b32_e32 v38, 63, v0
	v_mov_b32_e32 v29, 0xff800000
	v_cmp_gt_u32_e64 s[0:1], 32, v38
	s_waitcnt lgkmcnt(0)
	s_cmpk_gt_i32 s26, 0x600
	s_cselect_b64 s[24:25], -1, 0
	s_cmpk_lt_i32 s26, 0x601
	s_cbranch_scc1 .LBB4_6
	s_and_saveexec_b64 s[8:9], s[14:15]
	s_cbranch_execz .LBB4_5
	v_or_b32_e32 v178, s29, v0
	v_mov_b32_e32 v179, 0
	v_lshl_add_u64 v[178:179], v[178:179], 4, s[6:7]
	global_load_dwordx4 v[178:181], v[178:179], off
	v_lshlrev_b32_e32 v177, 4, v0
	s_waitcnt vmcnt(0)
	ds_write_b128 v177, v[178:181] offset:2080

.LBB4_39:
	s_waitcnt vmcnt(5)
	v_rcp_f32_e32 v2, v133
	s_waitcnt vmcnt(4)
	v_rcp_f32_e32 v3, v132
	s_waitcnt vmcnt(3)
	v_rcp_f32_e32 v4, v131
	v_cmp_lt_f32_e32 vcc, 0, v133
	s_waitcnt vmcnt(2)
	v_rcp_f32_e32 v5, v130
	s_waitcnt vmcnt(1)
	v_rcp_f32_e32 v6, v129
	v_cndmask_b32_e32 v2, 0, v2, vcc
	v_cmp_lt_f32_e32 vcc, 0, v132
	s_waitcnt vmcnt(0)
	v_rcp_f32_e32 v7, v128
	s_getpc_b64 s[36:37]
	s_sub_u32 s36, s36, 0x9238
	s_subb_u32 s37, s37, 0
	v_lshlrev_b32_e32 v183, 6, v0
	v_min_u32_e32 v183, 0x1980, v183
	global_load_dword v183, v183, s[36:37]
	v_lshlrev_b32_e32 v182, 6, v38
	global_load_dword v182, v182, s[38:39]
	s_mov_b32 s4, 0x42c80000
	v_cndmask_b32_e32 v3, 0, v3, vcc
	v_cmp_lt_f32_e32 vcc, 0, v131
	v_cmp_ngt_f32_e64 s[2:3], s4, v3
	s_mov_b64 s[6:7], 0
	v_cndmask_b32_e32 v4, 0, v4, vcc
	v_cmp_lt_f32_e32 vcc, 0, v130
	s_nop 1
	v_cndmask_b32_e32 v5, 0, v5, vcc
	v_cmp_lt_f32_e32 vcc, 0, v129
	s_nop 1
	v_cndmask_b32_e32 v6, 0, v6, vcc
	v_cmp_lt_f32_e32 vcc, 0, v128
	s_nop 1
	v_cndmask_b32_e32 v7, 0, v7, vcc
	v_cmp_ngt_f32_e32 vcc, s4, v2
	s_or_b64 s[2:3], vcc, s[2:3]
	v_cmp_ngt_f32_e32 vcc, s4, v4
	s_or_b64 s[2:3], s[2:3], vcc
	v_cmp_ngt_f32_e32 vcc, s4, v5
	s_or_b64 s[2:3], s[2:3], vcc
	v_cmp_ngt_f32_e32 vcc, s4, v6
	s_or_b64 s[2:3], s[2:3], vcc
	v_cmp_ngt_f32_e32 vcc, s4, v7
	s_or_b64 s[2:3], s[2:3], vcc
	v_cndmask_b32_e64 v8, 0, 1, s[2:3]
	v_cmp_ne_u32_e32 vcc, 0, v8
	s_cmp_eq_u64 vcc, 0
	s_cselect_b64 s[2:3], -1, 0
	v_cndmask_b32_e64 v8, 0, 1, s[2:3]
	s_nop 0
	v_readfirstlane_b32 s2, v8
	s_bitcmp0_b32 s2, 0
	s_cbranch_scc0 .LBB4_45
	s_cmp_lt_i32 s28, 4
	s_cbranch_scc1 .LBB4_46
	s_cmp_gt_i32 s28, 4
	s_cbranch_scc0 .LBB4_47
	s_mov_b64 s[4:5], -1
	v_mov_b32_e32 v8, 0
	s_cmp_gt_i32 s28, 5
	v_mov_b32_e32 v167, 0
	v_mov_b32_e32 v166, 0
	v_mov_b32_e32 v165, 0
	v_mov_b32_e32 v164, 0
	v_mov_b32_e32 v162, 0
	v_mov_b32_e32 v160, 0
	v_mov_b32_e32 v159, 0
	v_mov_b32_e32 v157, 0
	v_mov_b32_e32 v151, 0
	v_mov_b32_e32 v149, 0
	v_mov_b32_e32 v147, 0
	v_mov_b32_e32 v146, 0
	v_mov_b32_e32 v144, 0
	v_mov_b32_e32 v143, 0
	v_mov_b32_e32 v152, 0
	v_mov_b32_e32 v153, 0
	v_mov_b32_e32 v154, 0
	v_mov_b32_e32 v155, 0
	v_mov_b32_e32 v156, 0
	v_mov_b32_e32 v158, 0
	v_mov_b32_e32 v161, 0
	v_mov_b32_e32 v163, 0
	v_mov_b32_e32 v168, 0
	v_mov_b32_e32 v169, 0
	v_mov_b32_e32 v170, 0
	v_mov_b32_e32 v171, 0
	v_mov_b32_e32 v172, 0
	v_mov_b32_e32 v173, 0
	v_mov_b32_e32 v174, 0
	v_mov_b32_e32 v145, 0
	v_mov_b32_e32 v148, 0
	v_mov_b32_e32 v150, 0
	s_cbranch_scc0 .LBB4_50
	s_cmp_eq_u32 s28, 6
	s_cbranch_scc0 .LBB4_49
	v_mov_b32_e32 v145, 0
	v_mov_b32_e32 v148, 0
	v_mov_b32_e32 v150, 0
	v_mov_b32_e32 v143, 0
	v_mov_b32_e32 v144, 0
	v_mov_b32_e32 v146, 0
	v_mov_b32_e32 v147, 0
	v_mov_b32_e32 v149, 0
	v_mov_b32_e32 v151, 0
	v_mov_b32_e32 v152, 0
	v_mov_b32_e32 v153, 0
	v_mov_b32_e32 v154, 0
	v_mov_b32_e32 v155, 0
	v_mov_b32_e32 v156, 0
	v_mov_b32_e32 v158, 0
	v_mov_b32_e32 v161, 0
	v_mov_b32_e32 v163, 0
	v_mov_b32_e32 v157, 0
	v_mov_b32_e32 v159, 0
	v_mov_b32_e32 v160, 0
	v_mov_b32_e32 v162, 0
	v_mov_b32_e32 v164, 0
	v_mov_b32_e32 v165, 0
	v_mov_b32_e32 v166, 0
	v_mov_b32_e32 v167, 0
	v_mov_b32_e32 v168, 0
	v_mov_b32_e32 v169, 0
	v_mov_b32_e32 v170, 0
	v_mov_b32_e32 v171, 0
	v_mov_b32_e32 v172, 0
	v_mov_b32_e32 v173, 0
	v_mov_b32_e32 v174, 0
	v_fma_mix_f32 v148, v43, v7, v148 op_sel_hi:[1,0,0]
	v_fma_mix_f32 v150, v45, v7, v150 op_sel_hi:[1,0,0]
	v_fma_mix_f32 v143, v50, v7, v143 op_sel_hi:[1,0,0]
	v_fma_mix_f32 v144, v54, v7, v144 op_sel_hi:[1,0,0]
	v_fma_mix_f32 v146, v58, v7, v146 op_sel_hi:[1,0,0]
	v_fma_mix_f32 v147, v61, v7, v147 op_sel_hi:[1,0,0]
	v_fma_mix_f32 v149, v64, v7, v149 op_sel_hi:[1,0,0]
	v_fma_mix_f32 v151, v66, v7, v151 op_sel_hi:[1,0,0]
	v_fma_mix_f32 v152, v43, v7, v152 op_sel:[1,0,0] op_sel_hi:[1,0,0]
	v_fma_mix_f32 v153, v45, v7, v153 op_sel:[1,0,0] op_sel_hi:[1,0,0]
	v_fma_mix_f32 v154, v50, v7, v154 op_sel:[1,0,0] op_sel_hi:[1,0,0]
	v_fma_mix_f32 v155, v54, v7, v155 op_sel:[1,0,0] op_sel_hi:[1,0,0]
	v_fma_mix_f32 v156, v58, v7, v156 op_sel:[1,0,0] op_sel_hi:[1,0,0]
	v_fma_mix_f32 v158, v61, v7, v158 op_sel:[1,0,0] op_sel_hi:[1,0,0]
	v_fma_mix_f32 v161, v64, v7, v161 op_sel:[1,0,0] op_sel_hi:[1,0,0]
	v_fma_mix_f32 v163, v66, v7, v163 op_sel:[1,0,0] op_sel_hi:[1,0,0]
	v_fma_mix_f32 v157, v72, v7, v157 op_sel_hi:[1,0,0]
	v_fma_mix_f32 v159, v76, v7, v159 op_sel_hi:[1,0,0]
	v_fma_mix_f32 v160, v83, v7, v160 op_sel_hi:[1,0,0]
	v_fma_mix_f32 v162, v85, v7, v162 op_sel_hi:[1,0,0]
	v_fma_mix_f32 v164, v89, v7, v164 op_sel_hi:[1,0,0]
	v_fma_mix_f32 v165, v92, v7, v165 op_sel_hi:[1,0,0]
	v_fma_mix_f32 v166, v95, v7, v166 op_sel_hi:[1,0,0]
	v_fma_mix_f32 v167, v96, v7, v167 op_sel_hi:[1,0,0]
	v_fma_mix_f32 v168, v72, v7, v168 op_sel:[1,0,0] op_sel_hi:[1,0,0]
	v_fma_mix_f32 v169, v76, v7, v169 op_sel:[1,0,0] op_sel_hi:[1,0,0]
	v_fma_mix_f32 v170, v83, v7, v170 op_sel:[1,0,0] op_sel_hi:[1,0,0]
	v_fma_mix_f32 v171, v85, v7, v171 op_sel:[1,0,0] op_sel_hi:[1,0,0]
	v_fma_mix_f32 v172, v89, v7, v172 op_sel:[1,0,0] op_sel_hi:[1,0,0]
	v_fma_mix_f32 v173, v92, v7, v173 op_sel:[1,0,0] op_sel_hi:[1,0,0]
	v_fma_mix_f32 v174, v95, v7, v174 op_sel:[1,0,0] op_sel_hi:[1,0,0]
	v_fma_mix_f32 v145, v96, v7, v145 op_sel:[1,0,0] op_sel_hi:[1,0,0]
	s_branch .LBB4_50
